# baseline (speedup 1.0000x reference)
amdhsa.kernels:
  - .agpr_count:     32
    .args:
      - .actual_access:  read_only
        .address_space:  global
        .offset:         0
        .size:           8
        .value_kind:     global_buffer
      - .actual_access:  read_only
        .address_space:  global
        .offset:         8
        .size:           8
        .value_kind:     global_buffer
      - .actual_access:  read_only
        .address_space:  global
        .offset:         16
        .size:           8
        .value_kind:     global_buffer
      - .actual_access:  read_only
        .address_space:  global
        .offset:         24
        .size:           8
        .value_kind:     global_buffer
      - .actual_access:  write_only
        .address_space:  global
        .offset:         32
        .size:           8
        .value_kind:     global_buffer
      - .actual_access:  write_only
        .address_space:  global
        .offset:         40
        .size:           8
        .value_kind:     global_buffer
      - .actual_access:  write_only
        .address_space:  global
        .offset:         48
        .size:           8
        .value_kind:     global_buffer
      - .actual_access:  write_only
        .address_space:  global
        .offset:         56
        .size:           8
        .value_kind:     global_buffer
    .group_segment_fixed_size: 68352
    .kernarg_segment_align: 8
    .kernarg_segment_size: 64
    .language:       OpenCL C
    .language_version:
      - 2
      - 0
    .max_flat_workgroup_size: 256
    .name:           _Z6gat_k1PKfS0_S0_S0_PDF16_S1_S1_Pf
    .private_segment_fixed_size: 0
    .sgpr_count:     26
    .sgpr_spill_count: 0
    .symbol:         _Z6gat_k1PKfS0_S0_S0_PDF16_S1_S1_Pf.kd
    .uniform_work_group_size: 1
    .uses_dynamic_stack: false
    .vgpr_count:     156
    .vgpr_spill_count: 0
    .wavefront_size: 64
  - .agpr_count:     40
    .args:
      - .actual_access:  read_only
        .address_space:  global
        .offset:         0
        .size:           8
        .value_kind:     global_buffer
      - .actual_access:  read_only
        .address_space:  global
        .offset:         8
        .size:           8
        .value_kind:     global_buffer
      - .actual_access:  read_only
        .address_space:  global
        .offset:         16
        .size:           8
        .value_kind:     global_buffer
      - .actual_access:  read_only
        .address_space:  global
        .offset:         24
        .size:           8
        .value_kind:     global_buffer
      - .actual_access:  write_only
        .address_space:  global
        .offset:         32
        .size:           8
        .value_kind:     global_buffer
    .group_segment_fixed_size: 120832
    .kernarg_segment_align: 8
    .kernarg_segment_size: 40
    .language:       OpenCL C
    .language_version:
      - 2
      - 0
    .max_flat_workgroup_size: 512
    .name:           _Z6gat_k2PKDF16_S0_S0_PKfPf
    .private_segment_fixed_size: 0
    .sgpr_count:     38
    .sgpr_spill_count: 0
    .symbol:         _Z6gat_k2PKDF16_S0_S0_PKfPf.kd
    .uniform_work_group_size: 1
    .uses_dynamic_stack: false
    .vgpr_count:     216
    .vgpr_spill_count: 0
    .wavefront_size: 64
